# up-proj seam: first gate load no longer waited alone; P0 w_in items: the 8 waves of a WG take 8 adjacent column blocks (2 KB contiguous per source row); no stagger
# baseline (speedup 1.0000x reference)
.LBB0_13:
	s_lshr_b32 s92, s2, 6
	s_cmp_lt_i32 s62, 1
	v_writelane_b32 v254, s80, 4
	s_cselect_b64 s[0:1], -1, 0
	s_cmp_gt_i32 s63, 0
	v_writelane_b32 v254, s81, 5
	s_cselect_b64 s[4:5], -1, 0
	v_writelane_b32 v254, s91, 6
	s_mov_b64 s[6:7], s[62:63]
	s_and_b64 s[0:1], s[0:1], s[4:5]
	v_writelane_b32 v254, s4, 7
	s_andn2_b64 vcc, exec, s[0:1]
	s_mul_i32 s33, s92, 0x4100
	v_writelane_b32 v254, s5, 8
	v_writelane_b32 v254, s6, 9
	v_writelane_b32 v254, s7, 10
	s_cbranch_vccnz .LBB0_552
	s_mov_b64 s[24:25], s[80:81]
	v_mov_b32_e32 v0, 0
	s_and_b32 s4, s2, 0xffffffc0
	v_mbcnt_lo_u32_b32 v0, -1, v0
	v_mbcnt_hi_u32_b32 v0, -1, v0
	v_add_u32_e32 v67, s4, v0
	s_lshl_b32 s4, s93, 3
	s_add_i32 s52, s4, s92
	s_and_b32 s4, s52, 7
	s_bfe_u32 s5, s52, 0x30003
	s_andn2_b32 s52, s52, 63
	s_lshl_b32 s4, s4, 3
	s_or_b32 s52, s52, s4
	s_or_b32 s52, s52, s5
	s_cmpk_lt_i32 s52, 0x4e00
	s_cbranch_scc1 .LBB0_16
	s_lshl_b32 s54, s93, 9
	s_cbranch_execz .LBB0_17
	s_branch .LBB0_544
.LBB0_16:
.LBB0_17:
	v_and_b32_e32 v3, 15, v67
	v_bfe_u32 v71, v67, 4, 2
	s_add_i32 s4, s33, 0
	v_lshlrev_b32_e32 v2, 4, v3
	v_mul_u32_u24_e32 v4, 0x104, v71
	v_add3_u32 v180, s4, v2, v4
	v_lshlrev_b32_e32 v2, 3, v67
	v_bfe_u32 v181, v67, 3, 3
	v_and_b32_e32 v2, 56, v2
	v_and_b32_e32 v1, 63, v67
	v_mul_u32_u24_e32 v4, 0x104, v2
	v_lshlrev_b32_e32 v5, 2, v181
	v_and_b32_e32 v192, 3, v67
	v_add3_u32 v182, s4, v4, v5
	v_lshlrev_b32_e32 v66, 2, v1
	v_cmp_gt_u32_e64 s[8:9], 16, v1
	v_mul_u32_u24_e32 v1, 0x1040, v192
	v_and_b32_e32 v4, 60, v67
	v_add3_u32 v194, s4, v1, v4
	v_mov_b32_e32 v1, 0x1d00
	v_mov_b32_e32 v4, 0xd00
	v_cmp_gt_u32_e32 vcc, 4, v3
	s_lshl_b32 s6, s93, 6
	s_lshl_b32 s7, s92, 3
	v_lshlrev_b32_e32 v0, 2, v3
	v_mov_b32_e32 v65, 0
	v_bfe_u32 v193, v67, 2, 4
	v_cndmask_b32_e32 v1, v1, v4, vcc
	s_lshl_b32 s56, s52, 3
	s_lshl_b32 s54, s93, 9
	s_lshl_b32 s6, s92, 6
	s_lshl_b32 s53, s76, 3
	s_mov_b32 s27, 0
	v_or_b32_e32 v183, 8, v181
	v_or_b32_e32 v184, 16, v181
	v_or_b32_e32 v185, 24, v181
	v_or_b32_e32 v186, 32, v181
	v_or_b32_e32 v187, 40, v181
	v_or_b32_e32 v188, 48, v181
	v_or_b32_e32 v189, 56, v181
	v_xor_b32_e32 v190, 64, v66
	v_xor_b32_e32 v191, 0x80, v66
	v_lshlrev_b32_e32 v68, 4, v192
	v_mov_b32_e32 v69, v65
	v_or_b32_e32 v195, 16, v193
	v_or_b32_e32 v196, 32, v193
	v_or_b32_e32 v197, 48, v193
	v_cmp_gt_u32_e64 s[4:5], 6, v3
	v_or_b32_e32 v70, v1, v0
	s_and_b32 s55, s52, 7
	s_lshl_b32 s57, s76, 6
	s_lshl_b32 s58, s52, 6
	s_lshl_b32 s59, s76, 9
	s_add_i32 s60, s52, 0xffff9600
	s_mov_b64 s[28:29], 0xb0000
	s_mov_b32 s61, 0x2f800000
	s_mov_b32 s62, 0xcf800000
	s_mov_b32 s63, 0x90000
	s_mov_b32 s64, 0xb0000
	s_mov_b64 s[30:31], 0x14200000
	s_mov_b32 s65, 0xc3e00000
	s_mov_b64 s[34:35], 0x10200000
	s_mov_b32 s66, 0x10000
	s_mov_b32 s67, 0x20000
	s_mov_b32 s68, 0x30000
	s_mov_b32 s69, 0x40000
	s_mov_b32 s70, 0x50000
	s_mov_b32 s71, 0x60000
	s_mov_b32 s72, 0x70000
	s_mov_b32 s73, 0x80000
	s_mov_b32 s74, 0xa0000
	s_mov_b32 s75, 0xc0000
	s_mov_b32 s77, 0xd0000
	s_mov_b32 s78, 0xe0000
	s_mov_b32 s79, 0xf0000
	s_mov_b64 s[36:37], 0xd200000
	s_mov_b32 s80, 0x13460
	s_movk_i32 s81, 0xbc00
	s_movk_i32 s82, 0x2000
	s_mov_b64 s[38:39], 0x137000
	s_mov_b32 s83, 0x137000
	s_mov_b64 s[40:41], 0x200000
	s_mov_b32 s84, 0x40f00000
	s_brev_b32 s85, -2
	s_mov_b64 s[42:43], 0x2a00000
	s_movk_i32 s86, 0x60
	v_lshlrev_b32_e32 v72, 2, v0
	v_lshlrev_b32_e32 v74, 1, v2
	v_add_u32_e32 v198, 0x400, v182
	v_mov_b32_e32 v199, 0x43e00000
	v_mov_b32_e32 v200, 0x3e0293ee
	v_mov_b32_e32 v201, 0x3e000000
	v_mov_b32_e32 v202, 0x3e38aa3b
	v_mov_b32_e32 v203, 0x43000000
	v_mov_b32_e32 v204, 0x43800000
	v_mov_b32_e32 v205, 0x44800000
	v_mov_b32_e32 v206, 0x41000000
	v_mov_b32_e32 v207, 0x3e800000
	v_mov_b32_e32 v76, v65
	v_mov_b32_e32 v77, v65
	v_mov_b32_e32 v78, v65
	v_mov_b32_e32 v79, v65
	v_mov_b32_e32 v82, v65
	v_mov_b32_e32 v83, v65
	v_mov_b32_e32 v80, v65
	v_mov_b32_e32 v81, v65
	s_branch .LBB0_21

.LBB0_1635:
	s_andn2_b64 vcc, exec, s[50:51]
	s_cbranch_vccnz .LBB0_1637
	v_mov_b32_e32 v131, v205
	v_mov_b32_e32 v130, v214
	s_movk_i32 s10, 0xe000
	v_lshl_add_u32 v130, v130, 3, s66
	v_add_u32_e32 v217, s67, v131
	v_ashrrev_i32_e32 v131, 31, v130
	v_lshl_add_u64 v[130:131], v[130:131], 1, s[34:35]
	v_lshl_add_u64 v[130:131], s[8:9], 1, v[130:131]
	s_mov_b32 s11, -1
	v_lshl_add_u64 v[212:213], v[130:131], 0, s[10:11]
	v_mad_i64_i32 v[130:131], s[10:11], v217, s86, v[212:213]
	global_load_dwordx4 v[190:193], v[130:131], off
	v_add_co_u32_e32 v132, vcc, s33, v130
	s_nop 1
	v_addc_co_u32_e32 v133, vcc, 0, v131, vcc
	global_load_dwordx4 v[186:189], v[132:133], off
	global_load_dwordx4 v[182:185], v[130:131], off offset:256
	global_load_dwordx4 v[178:181], v[132:133], off offset:256
	v_add_u32_e32 v130, 16, v217
	v_mad_i64_i32 v[130:131], s[10:11], v130, s86, v[212:213]
	global_load_dwordx4 v[170:173], v[130:131], off
	v_add_co_u32_e32 v132, vcc, s33, v130
	s_nop 1
	v_addc_co_u32_e32 v133, vcc, 0, v131, vcc
	global_load_dwordx4 v[174:177], v[132:133], off
	global_load_dwordx4 v[166:169], v[130:131], off offset:256
	global_load_dwordx4 v[162:165], v[132:133], off offset:256
	v_add_u32_e32 v130, 32, v217
	v_mad_i64_i32 v[130:131], s[10:11], v130, s86, v[212:213]
	global_load_dwordx4 v[154:157], v[130:131], off
	v_add_co_u32_e32 v132, vcc, s33, v130
	s_nop 1
	v_addc_co_u32_e32 v133, vcc, 0, v131, vcc
	global_load_dwordx4 v[158:161], v[132:133], off
	global_load_dwordx4 v[138:141], v[130:131], off offset:256
	global_load_dwordx4 v[134:137], v[132:133], off offset:256
	v_add_u32_e32 v130, 48, v217
	v_mad_i64_i32 v[130:131], s[10:11], v130, s86, v[212:213]
	global_load_dwordx4 v[142:145], v[130:131], off
	v_add_co_u32_e32 v150, vcc, s33, v130
	s_nop 1
	v_addc_co_u32_e32 v151, vcc, 0, v131, vcc
	global_load_dwordx4 v[146:149], v[150:151], off
	s_nop 0
	global_load_dwordx4 v[130:133], v[130:131], off offset:256
	s_nop 0
	global_load_dwordx4 v[150:153], v[150:151], off offset:256
	s_waitcnt vmcnt(0)
	v_lshlrev_b32_e32 v202, 16, v190
	v_and_b32_e32 v190, 0xffff0000, v190
	v_add_f32_e32 v190, 1.0, v190
	v_rcp_f32_e32 v219, v190
	v_add_f32_e32 v202, 1.0, v202
	v_rcp_f32_e32 v218, v202
	v_lshlrev_b32_e32 v220, 16, v186
	v_and_b32_e32 v221, 0xffff0000, v186
	v_lshlrev_b32_e32 v186, 16, v191
	v_add_f32_e32 v186, 1.0, v186
	v_rcp_f32_e32 v190, v186
	v_and_b32_e32 v186, 0xffff0000, v191
	v_add_f32_e32 v186, 1.0, v186
	v_rcp_f32_e32 v191, v186
	v_lshlrev_b32_e32 v186, 16, v187
	v_and_b32_e32 v187, 0xffff0000, v187
	v_pk_add_f32 v[186:187], v[186:187], 1.0 op_sel_hi:[1,0]
	v_pk_add_f32 v[220:221], v[220:221], 1.0 op_sel_hi:[1,0]
	v_pk_mul_f32 v[186:187], v[186:187], v[190:191]
	v_lshlrev_b32_e32 v190, 16, v188
	v_pk_mul_f32 v[128:129], v[128:129], v[186:187]
	v_lshlrev_b32_e32 v186, 16, v192
	v_and_b32_e32 v187, 0xffff0000, v192
	v_add_f32_e32 v186, 1.0, v186
	v_add_f32_e32 v187, 1.0, v187
	v_rcp_f32_e32 v186, v186
	v_rcp_f32_e32 v187, v187
	v_and_b32_e32 v191, 0xffff0000, v188
	v_pk_add_f32 v[190:191], v[190:191], 1.0 op_sel_hi:[1,0]
	v_lshlrev_b32_e32 v188, 16, v189
	v_pk_mul_f32 v[186:187], v[190:191], v[186:187]
	v_and_b32_e32 v189, 0xffff0000, v189
	v_pk_mul_f32 v[122:123], v[122:123], v[186:187]
	v_lshlrev_b32_e32 v186, 16, v193
	v_and_b32_e32 v187, 0xffff0000, v193
	v_add_f32_e32 v186, 1.0, v186
	v_add_f32_e32 v187, 1.0, v187
	v_rcp_f32_e32 v186, v186
	v_rcp_f32_e32 v187, v187
	v_pk_add_f32 v[188:189], v[188:189], 1.0 op_sel_hi:[1,0]
	v_pk_mul_f32 v[218:219], v[220:221], v[218:219]
	v_pk_mul_f32 v[186:187], v[188:189], v[186:187]
	s_nop 0
	v_pk_mul_f32 v[124:125], v[124:125], v[186:187]
	v_lshlrev_b32_e32 v186, 16, v182
	v_and_b32_e32 v182, 0xffff0000, v182
	v_lshlrev_b32_e32 v188, 16, v178
	v_and_b32_e32 v189, 0xffff0000, v178
	v_lshlrev_b32_e32 v178, 16, v183
	v_add_f32_e32 v182, 1.0, v182
	v_add_f32_e32 v178, 1.0, v178
	v_rcp_f32_e32 v187, v182
	v_rcp_f32_e32 v182, v178
	v_and_b32_e32 v178, 0xffff0000, v183
	v_add_f32_e32 v178, 1.0, v178
	v_rcp_f32_e32 v183, v178
	v_lshlrev_b32_e32 v178, 16, v179
	v_and_b32_e32 v179, 0xffff0000, v179
	v_pk_add_f32 v[178:179], v[178:179], 1.0 op_sel_hi:[1,0]
	v_add_f32_e32 v186, 1.0, v186
	v_pk_mul_f32 v[178:179], v[178:179], v[182:183]
	v_lshlrev_b32_e32 v182, 16, v180
	v_pk_mul_f32 v[120:121], v[120:121], v[178:179]
	v_lshlrev_b32_e32 v178, 16, v184
	v_and_b32_e32 v179, 0xffff0000, v184
	v_add_f32_e32 v178, 1.0, v178
	v_add_f32_e32 v179, 1.0, v179
	v_rcp_f32_e32 v178, v178
	v_rcp_f32_e32 v179, v179
	v_and_b32_e32 v183, 0xffff0000, v180
	v_pk_add_f32 v[182:183], v[182:183], 1.0 op_sel_hi:[1,0]
	v_lshlrev_b32_e32 v180, 16, v181
	v_pk_mul_f32 v[178:179], v[182:183], v[178:179]
	v_and_b32_e32 v181, 0xffff0000, v181
	v_pk_mul_f32 v[114:115], v[114:115], v[178:179]
	v_lshlrev_b32_e32 v178, 16, v185
	v_and_b32_e32 v179, 0xffff0000, v185
	v_add_f32_e32 v178, 1.0, v178
	v_add_f32_e32 v179, 1.0, v179
	v_rcp_f32_e32 v178, v178
	v_rcp_f32_e32 v179, v179
	v_pk_add_f32 v[180:181], v[180:181], 1.0 op_sel_hi:[1,0]
	v_rcp_f32_e32 v186, v186
	v_pk_add_f32 v[188:189], v[188:189], 1.0 op_sel_hi:[1,0]
	v_pk_mul_f32 v[178:179], v[180:181], v[178:179]
	v_lshlrev_b32_e32 v180, 16, v174
	v_pk_mul_f32 v[116:117], v[116:117], v[178:179]
	v_lshlrev_b32_e32 v178, 16, v170
	v_and_b32_e32 v170, 0xffff0000, v170
	v_add_f32_e32 v170, 1.0, v170
	v_rcp_f32_e32 v179, v170
	v_lshlrev_b32_e32 v170, 16, v171
	v_and_b32_e32 v171, 0xffff0000, v171
	v_add_f32_e32 v170, 1.0, v170
	v_add_f32_e32 v171, 1.0, v171
	v_rcp_f32_e32 v170, v170
	v_rcp_f32_e32 v171, v171
	v_and_b32_e32 v181, 0xffff0000, v174
	v_lshlrev_b32_e32 v174, 16, v175
	v_and_b32_e32 v175, 0xffff0000, v175
	v_pk_add_f32 v[174:175], v[174:175], 1.0 op_sel_hi:[1,0]
	v_add_f32_e32 v178, 1.0, v178
	v_pk_mul_f32 v[170:171], v[174:175], v[170:171]
	v_lshlrev_b32_e32 v174, 16, v176
	v_pk_mul_f32 v[112:113], v[112:113], v[170:171]
	v_lshlrev_b32_e32 v170, 16, v172
	v_and_b32_e32 v171, 0xffff0000, v172
	v_add_f32_e32 v170, 1.0, v170
	v_add_f32_e32 v171, 1.0, v171
	v_rcp_f32_e32 v170, v170
	v_rcp_f32_e32 v171, v171
	v_and_b32_e32 v175, 0xffff0000, v176
	v_pk_add_f32 v[174:175], v[174:175], 1.0 op_sel_hi:[1,0]
	v_lshlrev_b32_e32 v172, 16, v177
	v_pk_mul_f32 v[170:171], v[174:175], v[170:171]
	v_rcp_f32_e32 v178, v178
	v_pk_mul_f32 v[106:107], v[106:107], v[170:171]
	v_lshlrev_b32_e32 v170, 16, v173
	v_and_b32_e32 v171, 0xffff0000, v173
	v_add_f32_e32 v170, 1.0, v170
	v_add_f32_e32 v171, 1.0, v171
	v_rcp_f32_e32 v170, v170
	v_rcp_f32_e32 v171, v171
	v_and_b32_e32 v173, 0xffff0000, v177
	v_pk_add_f32 v[172:173], v[172:173], 1.0 op_sel_hi:[1,0]
	v_pk_add_f32 v[180:181], v[180:181], 1.0 op_sel_hi:[1,0]
	v_pk_mul_f32 v[170:171], v[172:173], v[170:171]
	v_lshlrev_b32_e32 v172, 16, v162
	v_pk_mul_f32 v[108:109], v[108:109], v[170:171]
	v_lshlrev_b32_e32 v170, 16, v166
	v_and_b32_e32 v166, 0xffff0000, v166
	v_and_b32_e32 v173, 0xffff0000, v162
	v_lshlrev_b32_e32 v162, 16, v167
	v_add_f32_e32 v166, 1.0, v166
	v_add_f32_e32 v162, 1.0, v162
	v_rcp_f32_e32 v171, v166
	v_rcp_f32_e32 v166, v162
	v_and_b32_e32 v162, 0xffff0000, v167
	v_add_f32_e32 v162, 1.0, v162
	v_rcp_f32_e32 v167, v162
	v_lshlrev_b32_e32 v162, 16, v163
	v_and_b32_e32 v163, 0xffff0000, v163
	v_pk_add_f32 v[162:163], v[162:163], 1.0 op_sel_hi:[1,0]
	v_add_f32_e32 v170, 1.0, v170
	v_pk_mul_f32 v[162:163], v[162:163], v[166:167]
	v_lshlrev_b32_e32 v166, 16, v164
	v_pk_mul_f32 v[104:105], v[104:105], v[162:163]
	v_lshlrev_b32_e32 v162, 16, v168
	v_and_b32_e32 v163, 0xffff0000, v168
	v_add_f32_e32 v162, 1.0, v162
	v_add_f32_e32 v163, 1.0, v163
	v_rcp_f32_e32 v162, v162
	v_rcp_f32_e32 v163, v163
	v_and_b32_e32 v167, 0xffff0000, v164
	v_pk_add_f32 v[166:167], v[166:167], 1.0 op_sel_hi:[1,0]
	v_lshlrev_b32_e32 v164, 16, v165
	v_pk_mul_f32 v[162:163], v[166:167], v[162:163]
	v_and_b32_e32 v165, 0xffff0000, v165
	v_pk_mul_f32 v[98:99], v[98:99], v[162:163]
	v_lshlrev_b32_e32 v162, 16, v169
	v_and_b32_e32 v163, 0xffff0000, v169
	v_add_f32_e32 v162, 1.0, v162
	v_add_f32_e32 v163, 1.0, v163
	v_rcp_f32_e32 v162, v162
	v_rcp_f32_e32 v163, v163
	v_pk_add_f32 v[164:165], v[164:165], 1.0 op_sel_hi:[1,0]
	v_rcp_f32_e32 v170, v170
	v_pk_add_f32 v[172:173], v[172:173], 1.0 op_sel_hi:[1,0]
	v_pk_mul_f32 v[162:163], v[164:165], v[162:163]
	v_lshlrev_b32_e32 v164, 16, v158
	v_pk_mul_f32 v[100:101], v[100:101], v[162:163]
	v_lshlrev_b32_e32 v162, 16, v154
	v_and_b32_e32 v154, 0xffff0000, v154
	v_add_f32_e32 v154, 1.0, v154
	v_rcp_f32_e32 v163, v154
	v_lshlrev_b32_e32 v154, 16, v155
	v_and_b32_e32 v155, 0xffff0000, v155
	v_add_f32_e32 v154, 1.0, v154
	v_add_f32_e32 v155, 1.0, v155
	v_rcp_f32_e32 v154, v154
	v_rcp_f32_e32 v155, v155
	v_and_b32_e32 v165, 0xffff0000, v158
	v_lshlrev_b32_e32 v158, 16, v159
	v_and_b32_e32 v159, 0xffff0000, v159
	v_pk_add_f32 v[158:159], v[158:159], 1.0 op_sel_hi:[1,0]
	v_pk_mul_f32 v[170:171], v[172:173], v[170:171]
	v_pk_mul_f32 v[154:155], v[158:159], v[154:155]
	v_lshlrev_b32_e32 v158, 16, v160
	v_pk_mul_f32 v[96:97], v[96:97], v[154:155]
	v_lshlrev_b32_e32 v154, 16, v156
	v_and_b32_e32 v155, 0xffff0000, v156
	v_add_f32_e32 v154, 1.0, v154
	v_add_f32_e32 v155, 1.0, v155
	v_rcp_f32_e32 v154, v154
	v_rcp_f32_e32 v155, v155
	v_and_b32_e32 v159, 0xffff0000, v160
	v_pk_add_f32 v[158:159], v[158:159], 1.0 op_sel_hi:[1,0]
	v_lshlrev_b32_e32 v156, 16, v161
	v_pk_mul_f32 v[154:155], v[158:159], v[154:155]
	v_pk_mul_f32 v[102:103], v[102:103], v[170:171]
	v_pk_mul_f32 v[90:91], v[90:91], v[154:155]
	v_lshlrev_b32_e32 v154, 16, v157
	v_and_b32_e32 v155, 0xffff0000, v157
	v_add_f32_e32 v154, 1.0, v154
	v_add_f32_e32 v155, 1.0, v155
	v_rcp_f32_e32 v154, v154
	v_rcp_f32_e32 v155, v155
	v_and_b32_e32 v157, 0xffff0000, v161
	v_pk_add_f32 v[156:157], v[156:157], 1.0 op_sel_hi:[1,0]
	v_pk_mul_f32 v[178:179], v[180:181], v[178:179]
	v_pk_mul_f32 v[154:155], v[156:157], v[154:155]
	v_lshlrev_b32_e32 v156, 16, v134
	v_pk_mul_f32 v[92:93], v[92:93], v[154:155]
	v_lshlrev_b32_e32 v154, 16, v138
	v_and_b32_e32 v138, 0xffff0000, v138
	v_and_b32_e32 v157, 0xffff0000, v134
	v_lshlrev_b32_e32 v134, 16, v139
	v_add_f32_e32 v138, 1.0, v138
	v_add_f32_e32 v134, 1.0, v134
	v_rcp_f32_e32 v155, v138
	v_rcp_f32_e32 v138, v134
	v_and_b32_e32 v134, 0xffff0000, v139
	v_add_f32_e32 v134, 1.0, v134
	v_rcp_f32_e32 v139, v134
	v_lshlrev_b32_e32 v134, 16, v135
	v_and_b32_e32 v135, 0xffff0000, v135
	v_pk_add_f32 v[134:135], v[134:135], 1.0 op_sel_hi:[1,0]
	v_pk_mul_f32 v[110:111], v[110:111], v[178:179]
	v_pk_mul_f32 v[134:135], v[134:135], v[138:139]
	v_lshlrev_b32_e32 v138, 16, v136
	v_pk_mul_f32 v[88:89], v[88:89], v[134:135]
	v_lshlrev_b32_e32 v134, 16, v140
	v_and_b32_e32 v135, 0xffff0000, v140
	v_add_f32_e32 v134, 1.0, v134
	v_add_f32_e32 v135, 1.0, v135
	v_rcp_f32_e32 v134, v134
	v_rcp_f32_e32 v135, v135
	v_and_b32_e32 v139, 0xffff0000, v136
	v_pk_add_f32 v[138:139], v[138:139], 1.0 op_sel_hi:[1,0]
	v_lshlrev_b32_e32 v136, 16, v137
	v_pk_mul_f32 v[134:135], v[138:139], v[134:135]
	v_and_b32_e32 v137, 0xffff0000, v137
	v_pk_mul_f32 v[82:83], v[82:83], v[134:135]
	v_lshlrev_b32_e32 v134, 16, v141
	v_and_b32_e32 v135, 0xffff0000, v141
	v_add_f32_e32 v134, 1.0, v134
	v_add_f32_e32 v135, 1.0, v135
	v_rcp_f32_e32 v134, v134
	v_rcp_f32_e32 v135, v135
	v_pk_add_f32 v[136:137], v[136:137], 1.0 op_sel_hi:[1,0]
	v_pk_mul_f32 v[186:187], v[188:189], v[186:187]
	v_add_f32_e32 v162, 1.0, v162
	v_pk_mul_f32 v[134:135], v[136:137], v[134:135]
	v_lshlrev_b32_e32 v136, 16, v146
	v_pk_mul_f32 v[84:85], v[84:85], v[134:135]
	v_lshlrev_b32_e32 v134, 16, v142
	v_and_b32_e32 v135, 0xffff0000, v142
	v_add_f32_e32 v134, 1.0, v134
	v_add_f32_e32 v135, 1.0, v135
	v_rcp_f32_e32 v134, v134
	v_rcp_f32_e32 v135, v135
	v_and_b32_e32 v137, 0xffff0000, v146
	v_pk_add_f32 v[136:137], v[136:137], 1.0 op_sel_hi:[1,0]
	v_pk_mul_f32 v[118:119], v[118:119], v[186:187]
	v_pk_mul_f32 v[134:135], v[136:137], v[134:135]
	v_lshlrev_b32_e32 v136, 16, v147
	v_pk_mul_f32 v[78:79], v[78:79], v[134:135]
	v_lshlrev_b32_e32 v134, 16, v143
	v_and_b32_e32 v135, 0xffff0000, v143
	v_add_f32_e32 v134, 1.0, v134
	v_add_f32_e32 v135, 1.0, v135
	v_rcp_f32_e32 v134, v134
	v_rcp_f32_e32 v135, v135
	v_and_b32_e32 v137, 0xffff0000, v147
	v_pk_add_f32 v[136:137], v[136:137], 1.0 op_sel_hi:[1,0]
	v_rcp_f32_e32 v162, v162
	v_pk_mul_f32 v[134:135], v[136:137], v[134:135]
	v_lshlrev_b32_e32 v136, 16, v148
	v_pk_mul_f32 v[80:81], v[80:81], v[134:135]
	v_lshlrev_b32_e32 v134, 16, v144
	v_and_b32_e32 v135, 0xffff0000, v144
	v_add_f32_e32 v134, 1.0, v134
	v_add_f32_e32 v135, 1.0, v135
	v_rcp_f32_e32 v134, v134
	v_rcp_f32_e32 v135, v135
	v_and_b32_e32 v137, 0xffff0000, v148
	v_pk_add_f32 v[136:137], v[136:137], 1.0 op_sel_hi:[1,0]
	v_pk_add_f32 v[164:165], v[164:165], 1.0 op_sel_hi:[1,0]
	v_pk_mul_f32 v[134:135], v[136:137], v[134:135]
	v_lshlrev_b32_e32 v136, 16, v149
	v_pk_mul_f32 v[74:75], v[74:75], v[134:135]
	v_lshlrev_b32_e32 v134, 16, v145
	v_and_b32_e32 v135, 0xffff0000, v145
	v_add_f32_e32 v134, 1.0, v134
	v_add_f32_e32 v135, 1.0, v135
	v_rcp_f32_e32 v134, v134
	v_rcp_f32_e32 v135, v135
	v_and_b32_e32 v137, 0xffff0000, v149
	v_pk_add_f32 v[136:137], v[136:137], 1.0 op_sel_hi:[1,0]
	v_pk_mul_f32 v[162:163], v[164:165], v[162:163]
	v_pk_mul_f32 v[134:135], v[136:137], v[134:135]
	v_lshlrev_b32_e32 v136, 16, v150
	v_pk_mul_f32 v[76:77], v[76:77], v[134:135]
	v_lshlrev_b32_e32 v134, 16, v130
	v_and_b32_e32 v130, 0xffff0000, v130
	v_add_f32_e32 v134, 1.0, v134
	v_add_f32_e32 v130, 1.0, v130
	v_rcp_f32_e32 v134, v134
	v_rcp_f32_e32 v135, v130
	v_lshlrev_b32_e32 v130, 16, v131
	v_and_b32_e32 v131, 0xffff0000, v131
	v_and_b32_e32 v137, 0xffff0000, v150
	v_add_f32_e32 v130, 1.0, v130
	v_add_f32_e32 v131, 1.0, v131
	v_pk_add_f32 v[136:137], v[136:137], 1.0 op_sel_hi:[1,0]
	v_rcp_f32_e32 v130, v130
	v_rcp_f32_e32 v131, v131
	v_pk_mul_f32 v[134:135], v[136:137], v[134:135]
	v_pk_mul_f32 v[94:95], v[94:95], v[162:163]
	v_pk_mul_f32 v[70:71], v[70:71], v[134:135]
	v_lshlrev_b32_e32 v134, 16, v151
	v_and_b32_e32 v135, 0xffff0000, v151
	v_pk_add_f32 v[134:135], v[134:135], 1.0 op_sel_hi:[1,0]
	v_add_f32_e32 v154, 1.0, v154
	v_pk_mul_f32 v[130:131], v[134:135], v[130:131]
	v_lshlrev_b32_e32 v134, 16, v152
	v_pk_mul_f32 v[72:73], v[72:73], v[130:131]
	v_lshlrev_b32_e32 v130, 16, v132
	v_and_b32_e32 v131, 0xffff0000, v132
	v_add_f32_e32 v130, 1.0, v130
	v_add_f32_e32 v131, 1.0, v131
	v_rcp_f32_e32 v130, v130
	v_rcp_f32_e32 v131, v131
	v_and_b32_e32 v135, 0xffff0000, v152
	v_pk_add_f32 v[134:135], v[134:135], 1.0 op_sel_hi:[1,0]
	v_lshlrev_b32_e32 v132, 16, v153
	v_pk_mul_f32 v[130:131], v[134:135], v[130:131]
	v_rcp_f32_e32 v154, v154
	v_pk_mul_f32 v[66:67], v[66:67], v[130:131]
	v_lshlrev_b32_e32 v130, 16, v133
	v_and_b32_e32 v131, 0xffff0000, v133
	v_add_f32_e32 v130, 1.0, v130
	v_add_f32_e32 v131, 1.0, v131
	v_rcp_f32_e32 v130, v130
	v_rcp_f32_e32 v131, v131
	v_and_b32_e32 v133, 0xffff0000, v153
	v_pk_add_f32 v[132:133], v[132:133], 1.0 op_sel_hi:[1,0]
	v_pk_add_f32 v[156:157], v[156:157], 1.0 op_sel_hi:[1,0]
	v_pk_mul_f32 v[130:131], v[132:133], v[130:131]
	v_pk_mul_f32 v[154:155], v[156:157], v[154:155]
	v_pk_mul_f32 v[68:69], v[68:69], v[130:131]
	v_add_u32_e32 v130, 0x80, v217
	v_mad_i64_i32 v[130:131], s[10:11], v130, s86, v[212:213]
	global_load_dwordx4 v[170:173], v[130:131], off
	v_add_co_u32_e32 v132, vcc, s33, v130
	v_pk_mul_f32 v[86:87], v[86:87], v[154:155]
	s_nop 0
	v_addc_co_u32_e32 v133, vcc, 0, v131, vcc
	global_load_dwordx4 v[174:177], v[132:133], off
	global_load_dwordx4 v[178:181], v[130:131], off offset:256
	global_load_dwordx4 v[182:185], v[132:133], off offset:256
	v_add_u32_e32 v130, 0x90, v217
	v_mad_i64_i32 v[130:131], s[10:11], v130, s86, v[212:213]
	global_load_dwordx4 v[186:189], v[130:131], off
	v_add_co_u32_e32 v132, vcc, s33, v130
	v_pk_mul_f32 v[126:127], v[126:127], v[218:219]
	s_nop 0
	v_addc_co_u32_e32 v133, vcc, 0, v131, vcc
	global_load_dwordx4 v[190:193], v[132:133], off
	global_load_dwordx4 v[162:165], v[130:131], off offset:256
	global_load_dwordx4 v[166:169], v[132:133], off offset:256
	v_add_u32_e32 v130, 0xa0, v217
	v_mad_i64_i32 v[130:131], s[10:11], v130, s86, v[212:213]
	v_add_co_u32_e32 v132, vcc, s33, v130
	global_load_dwordx4 v[154:157], v[130:131], off
	s_nop 0
	v_addc_co_u32_e32 v133, vcc, 0, v131, vcc
	global_load_dwordx4 v[158:161], v[132:133], off
	global_load_dwordx4 v[146:149], v[130:131], off offset:256
	global_load_dwordx4 v[150:153], v[132:133], off offset:256
	v_add_u32_e32 v130, 0xb0, v217
	v_mad_i64_i32 v[130:131], s[10:11], v130, s86, v[212:213]
	global_load_dwordx4 v[138:141], v[130:131], off
	v_add_co_u32_e32 v134, vcc, s33, v130
	s_waitcnt vmcnt(0)
	v_lshlrev_b32_e32 v202, 16, v170
	v_and_b32_e32 v170, 0xffff0000, v170
	v_add_f32_e32 v170, 1.0, v170
	v_rcp_f32_e32 v213, v170
	v_lshlrev_b32_e32 v170, 16, v171
	v_and_b32_e32 v171, 0xffff0000, v171
	v_add_f32_e32 v170, 1.0, v170
	v_add_f32_e32 v171, 1.0, v171
	v_rcp_f32_e32 v170, v170
	v_rcp_f32_e32 v171, v171
	v_lshlrev_b32_e32 v218, 16, v174
	v_and_b32_e32 v219, 0xffff0000, v174
	v_lshlrev_b32_e32 v174, 16, v175
	v_and_b32_e32 v175, 0xffff0000, v175
	v_pk_add_f32 v[174:175], v[174:175], 1.0 op_sel_hi:[1,0]
	v_addc_co_u32_e32 v135, vcc, 0, v131, vcc
	v_pk_mul_f32 v[170:171], v[174:175], v[170:171]
	v_lshlrev_b32_e32 v174, 16, v176
	v_pk_mul_f32 v[64:65], v[64:65], v[170:171]
	v_lshlrev_b32_e32 v170, 16, v172
	v_and_b32_e32 v171, 0xffff0000, v172
	v_add_f32_e32 v170, 1.0, v170
	v_add_f32_e32 v171, 1.0, v171
	v_rcp_f32_e32 v170, v170
	v_rcp_f32_e32 v171, v171
	v_and_b32_e32 v175, 0xffff0000, v176
	v_pk_add_f32 v[174:175], v[174:175], 1.0 op_sel_hi:[1,0]
	v_lshlrev_b32_e32 v172, 16, v177
	v_pk_mul_f32 v[170:171], v[174:175], v[170:171]
	global_load_dwordx4 v[142:145], v[134:135], off
	s_nop 0
	global_load_dwordx4 v[130:133], v[130:131], off offset:256
	s_nop 0
	global_load_dwordx4 v[134:137], v[134:135], off offset:256
	v_pk_mul_f32 v[58:59], v[58:59], v[170:171]
	v_lshlrev_b32_e32 v170, 16, v173
	v_and_b32_e32 v171, 0xffff0000, v173
	v_add_f32_e32 v170, 1.0, v170
	v_add_f32_e32 v171, 1.0, v171
	v_rcp_f32_e32 v170, v170
	v_rcp_f32_e32 v171, v171
	v_and_b32_e32 v173, 0xffff0000, v177
	v_pk_add_f32 v[172:173], v[172:173], 1.0 op_sel_hi:[1,0]
	v_add_f32_e32 v202, 1.0, v202
	v_pk_mul_f32 v[170:171], v[172:173], v[170:171]
	v_lshlrev_b32_e32 v172, 16, v182
	v_pk_mul_f32 v[60:61], v[60:61], v[170:171]
	v_lshlrev_b32_e32 v170, 16, v178
	v_and_b32_e32 v171, 0xffff0000, v178
	v_add_f32_e32 v170, 1.0, v170
	v_add_f32_e32 v171, 1.0, v171
	v_rcp_f32_e32 v170, v170
	v_rcp_f32_e32 v171, v171
	v_and_b32_e32 v173, 0xffff0000, v182
	v_pk_add_f32 v[172:173], v[172:173], 1.0 op_sel_hi:[1,0]
	v_rcp_f32_e32 v212, v202
	v_pk_mul_f32 v[170:171], v[172:173], v[170:171]
	v_lshlrev_b32_e32 v172, 16, v183
	v_pk_mul_f32 v[54:55], v[54:55], v[170:171]
	v_lshlrev_b32_e32 v170, 16, v179
	v_and_b32_e32 v171, 0xffff0000, v179
	v_add_f32_e32 v170, 1.0, v170
	v_add_f32_e32 v171, 1.0, v171
	v_rcp_f32_e32 v170, v170
	v_rcp_f32_e32 v171, v171
	v_and_b32_e32 v173, 0xffff0000, v183
	v_pk_add_f32 v[172:173], v[172:173], 1.0 op_sel_hi:[1,0]
	v_pk_add_f32 v[218:219], v[218:219], 1.0 op_sel_hi:[1,0]
	v_pk_mul_f32 v[170:171], v[172:173], v[170:171]
	v_lshlrev_b32_e32 v172, 16, v184
	v_pk_mul_f32 v[56:57], v[56:57], v[170:171]
	v_lshlrev_b32_e32 v170, 16, v180
	v_and_b32_e32 v171, 0xffff0000, v180
	v_add_f32_e32 v170, 1.0, v170
	v_add_f32_e32 v171, 1.0, v171
	v_rcp_f32_e32 v170, v170
	v_rcp_f32_e32 v171, v171
	v_and_b32_e32 v173, 0xffff0000, v184
	v_pk_add_f32 v[172:173], v[172:173], 1.0 op_sel_hi:[1,0]
	v_pk_mul_f32 v[212:213], v[218:219], v[212:213]
	v_pk_mul_f32 v[170:171], v[172:173], v[170:171]
	v_lshlrev_b32_e32 v172, 16, v185
	v_pk_mul_f32 v[50:51], v[50:51], v[170:171]
	v_lshlrev_b32_e32 v170, 16, v181
	v_and_b32_e32 v171, 0xffff0000, v181
	v_add_f32_e32 v170, 1.0, v170
	v_add_f32_e32 v171, 1.0, v171
	v_rcp_f32_e32 v170, v170
	v_rcp_f32_e32 v171, v171
	v_and_b32_e32 v173, 0xffff0000, v185
	v_pk_add_f32 v[172:173], v[172:173], 1.0 op_sel_hi:[1,0]
	v_pk_mul_f32 v[62:63], v[62:63], v[212:213]
	v_pk_mul_f32 v[170:171], v[172:173], v[170:171]
	v_lshlrev_b32_e32 v172, 16, v190
	v_pk_mul_f32 v[52:53], v[52:53], v[170:171]
	v_lshlrev_b32_e32 v170, 16, v186
	v_and_b32_e32 v171, 0xffff0000, v186
	v_add_f32_e32 v170, 1.0, v170
	v_add_f32_e32 v171, 1.0, v171
	v_rcp_f32_e32 v170, v170
	v_rcp_f32_e32 v171, v171
	v_and_b32_e32 v173, 0xffff0000, v190
	v_pk_add_f32 v[172:173], v[172:173], 1.0 op_sel_hi:[1,0]
	s_nop 0
	v_pk_mul_f32 v[170:171], v[172:173], v[170:171]
	v_lshlrev_b32_e32 v172, 16, v191
	v_pk_mul_f32 v[46:47], v[46:47], v[170:171]
	v_lshlrev_b32_e32 v170, 16, v187
	v_and_b32_e32 v171, 0xffff0000, v187
	v_add_f32_e32 v170, 1.0, v170
	v_add_f32_e32 v171, 1.0, v171
	v_rcp_f32_e32 v170, v170
	v_rcp_f32_e32 v171, v171
	v_and_b32_e32 v173, 0xffff0000, v191
	v_pk_add_f32 v[172:173], v[172:173], 1.0 op_sel_hi:[1,0]
	s_nop 0
	v_pk_mul_f32 v[170:171], v[172:173], v[170:171]
	v_lshlrev_b32_e32 v172, 16, v192
	v_pk_mul_f32 v[48:49], v[48:49], v[170:171]
	v_lshlrev_b32_e32 v170, 16, v188
	v_and_b32_e32 v171, 0xffff0000, v188
	v_add_f32_e32 v170, 1.0, v170
	v_add_f32_e32 v171, 1.0, v171
	v_rcp_f32_e32 v170, v170
	v_rcp_f32_e32 v171, v171
	v_and_b32_e32 v173, 0xffff0000, v192
	v_pk_add_f32 v[172:173], v[172:173], 1.0 op_sel_hi:[1,0]
	s_nop 0
	v_pk_mul_f32 v[170:171], v[172:173], v[170:171]
	v_lshlrev_b32_e32 v172, 16, v193
	v_pk_mul_f32 v[42:43], v[42:43], v[170:171]
	v_lshlrev_b32_e32 v170, 16, v189
	v_and_b32_e32 v171, 0xffff0000, v189
	v_add_f32_e32 v170, 1.0, v170
	v_add_f32_e32 v171, 1.0, v171
	v_rcp_f32_e32 v170, v170
	v_rcp_f32_e32 v171, v171
	v_and_b32_e32 v173, 0xffff0000, v193
	v_pk_add_f32 v[172:173], v[172:173], 1.0 op_sel_hi:[1,0]
	s_nop 0
	v_pk_mul_f32 v[170:171], v[172:173], v[170:171]
	v_lshlrev_b32_e32 v172, 16, v166
	v_pk_mul_f32 v[44:45], v[44:45], v[170:171]
	v_lshlrev_b32_e32 v170, 16, v162
	v_and_b32_e32 v162, 0xffff0000, v162
	v_add_f32_e32 v162, 1.0, v162
	v_rcp_f32_e32 v171, v162
	v_lshlrev_b32_e32 v162, 16, v163
	v_and_b32_e32 v163, 0xffff0000, v163
	v_add_f32_e32 v162, 1.0, v162
	v_add_f32_e32 v163, 1.0, v163
	v_rcp_f32_e32 v162, v162
	v_rcp_f32_e32 v163, v163
	v_and_b32_e32 v173, 0xffff0000, v166
	v_lshlrev_b32_e32 v166, 16, v167
	v_and_b32_e32 v167, 0xffff0000, v167
	v_pk_add_f32 v[166:167], v[166:167], 1.0 op_sel_hi:[1,0]
	v_add_f32_e32 v170, 1.0, v170
	v_pk_mul_f32 v[162:163], v[166:167], v[162:163]
	v_lshlrev_b32_e32 v166, 16, v168
	v_pk_mul_f32 v[40:41], v[40:41], v[162:163]
	v_lshlrev_b32_e32 v162, 16, v164
	v_and_b32_e32 v163, 0xffff0000, v164
	v_add_f32_e32 v162, 1.0, v162
	v_add_f32_e32 v163, 1.0, v163
	v_rcp_f32_e32 v162, v162
	v_rcp_f32_e32 v163, v163
	v_and_b32_e32 v167, 0xffff0000, v168
	v_pk_add_f32 v[166:167], v[166:167], 1.0 op_sel_hi:[1,0]
	v_lshlrev_b32_e32 v164, 16, v169
	v_pk_mul_f32 v[162:163], v[166:167], v[162:163]
	v_rcp_f32_e32 v170, v170
	v_pk_mul_f32 v[34:35], v[34:35], v[162:163]
	v_lshlrev_b32_e32 v162, 16, v165
	v_and_b32_e32 v163, 0xffff0000, v165
	v_add_f32_e32 v162, 1.0, v162
	v_add_f32_e32 v163, 1.0, v163
	v_rcp_f32_e32 v162, v162
	v_rcp_f32_e32 v163, v163
	v_and_b32_e32 v165, 0xffff0000, v169
	v_pk_add_f32 v[164:165], v[164:165], 1.0 op_sel_hi:[1,0]
	v_pk_add_f32 v[172:173], v[172:173], 1.0 op_sel_hi:[1,0]
	v_pk_mul_f32 v[162:163], v[164:165], v[162:163]
	v_lshlrev_b32_e32 v164, 16, v158
	v_pk_mul_f32 v[36:37], v[36:37], v[162:163]
	v_lshlrev_b32_e32 v162, 16, v154
	v_and_b32_e32 v154, 0xffff0000, v154
	v_add_f32_e32 v154, 1.0, v154
	v_rcp_f32_e32 v163, v154
	v_lshlrev_b32_e32 v154, 16, v155
	v_and_b32_e32 v155, 0xffff0000, v155
	v_add_f32_e32 v154, 1.0, v154
	v_add_f32_e32 v155, 1.0, v155
	v_rcp_f32_e32 v154, v154
	v_rcp_f32_e32 v155, v155
	v_and_b32_e32 v165, 0xffff0000, v158
	v_lshlrev_b32_e32 v158, 16, v159
	v_and_b32_e32 v159, 0xffff0000, v159
	v_pk_add_f32 v[158:159], v[158:159], 1.0 op_sel_hi:[1,0]
	v_add_f32_e32 v162, 1.0, v162
	v_pk_mul_f32 v[154:155], v[158:159], v[154:155]
	v_lshlrev_b32_e32 v158, 16, v160
	v_pk_mul_f32 v[32:33], v[32:33], v[154:155]
	v_lshlrev_b32_e32 v154, 16, v156
	v_and_b32_e32 v155, 0xffff0000, v156
	v_add_f32_e32 v154, 1.0, v154
	v_add_f32_e32 v155, 1.0, v155
	v_rcp_f32_e32 v154, v154
	v_rcp_f32_e32 v155, v155
	v_and_b32_e32 v159, 0xffff0000, v160
	v_pk_add_f32 v[158:159], v[158:159], 1.0 op_sel_hi:[1,0]
	v_lshlrev_b32_e32 v156, 16, v161
	v_pk_mul_f32 v[154:155], v[158:159], v[154:155]
	v_rcp_f32_e32 v162, v162
	v_pk_mul_f32 v[26:27], v[26:27], v[154:155]
	v_lshlrev_b32_e32 v154, 16, v157
	v_and_b32_e32 v155, 0xffff0000, v157
	v_add_f32_e32 v154, 1.0, v154
	v_add_f32_e32 v155, 1.0, v155
	v_rcp_f32_e32 v154, v154
	v_rcp_f32_e32 v155, v155
	v_and_b32_e32 v157, 0xffff0000, v161
	v_pk_add_f32 v[156:157], v[156:157], 1.0 op_sel_hi:[1,0]
	v_pk_add_f32 v[164:165], v[164:165], 1.0 op_sel_hi:[1,0]
	v_pk_mul_f32 v[154:155], v[156:157], v[154:155]
	v_lshlrev_b32_e32 v156, 16, v150
	v_pk_mul_f32 v[28:29], v[28:29], v[154:155]
	v_lshlrev_b32_e32 v154, 16, v146
	v_and_b32_e32 v146, 0xffff0000, v146
	v_add_f32_e32 v146, 1.0, v146
	v_rcp_f32_e32 v155, v146
	v_lshlrev_b32_e32 v146, 16, v147
	v_and_b32_e32 v147, 0xffff0000, v147
	v_add_f32_e32 v146, 1.0, v146
	v_add_f32_e32 v147, 1.0, v147
	v_rcp_f32_e32 v146, v146
	v_rcp_f32_e32 v147, v147
	v_and_b32_e32 v157, 0xffff0000, v150
	v_lshlrev_b32_e32 v150, 16, v151
	v_and_b32_e32 v151, 0xffff0000, v151
	v_pk_add_f32 v[150:151], v[150:151], 1.0 op_sel_hi:[1,0]
	v_add_f32_e32 v154, 1.0, v154
	v_pk_mul_f32 v[146:147], v[150:151], v[146:147]
	v_lshlrev_b32_e32 v150, 16, v152
	v_pk_mul_f32 v[24:25], v[24:25], v[146:147]
	v_lshlrev_b32_e32 v146, 16, v148
	v_and_b32_e32 v147, 0xffff0000, v148
	v_add_f32_e32 v146, 1.0, v146
	v_add_f32_e32 v147, 1.0, v147
	v_rcp_f32_e32 v146, v146
	v_rcp_f32_e32 v147, v147
	v_and_b32_e32 v151, 0xffff0000, v152
	v_pk_add_f32 v[150:151], v[150:151], 1.0 op_sel_hi:[1,0]
	v_lshlrev_b32_e32 v148, 16, v153
	v_pk_mul_f32 v[146:147], v[150:151], v[146:147]
	v_rcp_f32_e32 v154, v154
	v_pk_mul_f32 v[18:19], v[18:19], v[146:147]
	v_lshlrev_b32_e32 v146, 16, v149
	v_and_b32_e32 v147, 0xffff0000, v149
	v_add_f32_e32 v146, 1.0, v146
	v_add_f32_e32 v147, 1.0, v147
	v_rcp_f32_e32 v146, v146
	v_rcp_f32_e32 v147, v147
	v_and_b32_e32 v149, 0xffff0000, v153
	v_pk_add_f32 v[148:149], v[148:149], 1.0 op_sel_hi:[1,0]
	v_pk_add_f32 v[156:157], v[156:157], 1.0 op_sel_hi:[1,0]
	v_pk_mul_f32 v[146:147], v[148:149], v[146:147]
	s_waitcnt vmcnt(0)
	v_lshlrev_b32_e32 v148, 16, v142
	v_pk_mul_f32 v[20:21], v[20:21], v[146:147]
	v_lshlrev_b32_e32 v146, 16, v138
	v_and_b32_e32 v138, 0xffff0000, v138
	v_add_f32_e32 v138, 1.0, v138
	v_rcp_f32_e32 v147, v138
	v_lshlrev_b32_e32 v138, 16, v139
	v_and_b32_e32 v139, 0xffff0000, v139
	v_add_f32_e32 v138, 1.0, v138
	v_add_f32_e32 v139, 1.0, v139
	v_rcp_f32_e32 v138, v138
	v_rcp_f32_e32 v139, v139
	v_and_b32_e32 v149, 0xffff0000, v142
	v_lshlrev_b32_e32 v142, 16, v143
	v_and_b32_e32 v143, 0xffff0000, v143
	v_pk_add_f32 v[142:143], v[142:143], 1.0 op_sel_hi:[1,0]
	v_add_f32_e32 v146, 1.0, v146
	v_pk_mul_f32 v[138:139], v[142:143], v[138:139]
	v_lshlrev_b32_e32 v142, 16, v144
	v_pk_mul_f32 v[16:17], v[16:17], v[138:139]
	v_lshlrev_b32_e32 v138, 16, v140
	v_and_b32_e32 v139, 0xffff0000, v140
	v_add_f32_e32 v138, 1.0, v138
	v_add_f32_e32 v139, 1.0, v139
	v_rcp_f32_e32 v138, v138
	v_rcp_f32_e32 v139, v139
	v_and_b32_e32 v143, 0xffff0000, v144
	v_pk_add_f32 v[142:143], v[142:143], 1.0 op_sel_hi:[1,0]
	v_lshlrev_b32_e32 v140, 16, v145
	v_pk_mul_f32 v[138:139], v[142:143], v[138:139]
	v_rcp_f32_e32 v146, v146
	v_pk_mul_f32 v[10:11], v[10:11], v[138:139]
	v_lshlrev_b32_e32 v138, 16, v141
	v_and_b32_e32 v139, 0xffff0000, v141
	v_add_f32_e32 v138, 1.0, v138
	v_add_f32_e32 v139, 1.0, v139
	v_rcp_f32_e32 v138, v138
	v_rcp_f32_e32 v139, v139
	v_and_b32_e32 v141, 0xffff0000, v145
	v_pk_add_f32 v[140:141], v[140:141], 1.0 op_sel_hi:[1,0]
	v_pk_add_f32 v[148:149], v[148:149], 1.0 op_sel_hi:[1,0]
	v_pk_mul_f32 v[138:139], v[140:141], v[138:139]
	v_lshlrev_b32_e32 v140, 16, v134
	v_pk_mul_f32 v[12:13], v[12:13], v[138:139]
	v_lshlrev_b32_e32 v138, 16, v130
	v_and_b32_e32 v130, 0xffff0000, v130
	v_add_f32_e32 v130, 1.0, v130
	v_rcp_f32_e32 v139, v130
	v_lshlrev_b32_e32 v130, 16, v131
	v_and_b32_e32 v131, 0xffff0000, v131
	v_add_f32_e32 v130, 1.0, v130
	v_add_f32_e32 v131, 1.0, v131
	v_rcp_f32_e32 v130, v130
	v_rcp_f32_e32 v131, v131
	v_and_b32_e32 v141, 0xffff0000, v134
	v_lshlrev_b32_e32 v134, 16, v135
	v_and_b32_e32 v135, 0xffff0000, v135
	v_pk_add_f32 v[134:135], v[134:135], 1.0 op_sel_hi:[1,0]
	v_add_f32_e32 v138, 1.0, v138
	v_pk_mul_f32 v[130:131], v[134:135], v[130:131]
	v_lshlrev_b32_e32 v134, 16, v136
	v_pk_mul_f32 v[8:9], v[8:9], v[130:131]
	v_lshlrev_b32_e32 v130, 16, v132
	v_and_b32_e32 v131, 0xffff0000, v132
	v_add_f32_e32 v130, 1.0, v130
	v_add_f32_e32 v131, 1.0, v131
	v_rcp_f32_e32 v130, v130
	v_rcp_f32_e32 v131, v131
	v_and_b32_e32 v135, 0xffff0000, v136
	v_pk_add_f32 v[134:135], v[134:135], 1.0 op_sel_hi:[1,0]
	v_rcp_f32_e32 v138, v138
	v_pk_mul_f32 v[130:131], v[134:135], v[130:131]
	v_lshlrev_b32_e32 v132, 16, v137
	v_pk_mul_f32 v[2:3], v[2:3], v[130:131]
	v_lshlrev_b32_e32 v130, 16, v133
	v_and_b32_e32 v131, 0xffff0000, v133
	v_add_f32_e32 v130, 1.0, v130
	v_add_f32_e32 v131, 1.0, v131
	v_rcp_f32_e32 v130, v130
	v_rcp_f32_e32 v131, v131
	v_and_b32_e32 v133, 0xffff0000, v137
	v_pk_add_f32 v[140:141], v[140:141], 1.0 op_sel_hi:[1,0]
	v_pk_add_f32 v[132:133], v[132:133], 1.0 op_sel_hi:[1,0]
	v_pk_mul_f32 v[170:171], v[172:173], v[170:171]
	v_pk_mul_f32 v[162:163], v[164:165], v[162:163]
	v_pk_mul_f32 v[154:155], v[156:157], v[154:155]
	v_pk_mul_f32 v[146:147], v[148:149], v[146:147]
	v_pk_mul_f32 v[138:139], v[140:141], v[138:139]
	v_pk_mul_f32 v[130:131], v[132:133], v[130:131]
	v_pk_mul_f32 v[38:39], v[38:39], v[170:171]
	v_pk_mul_f32 v[30:31], v[30:31], v[162:163]
	v_pk_mul_f32 v[22:23], v[22:23], v[154:155]
	v_pk_mul_f32 v[14:15], v[14:15], v[146:147]
	v_pk_mul_f32 v[6:7], v[6:7], v[138:139]
	v_pk_mul_f32 v[4:5], v[4:5], v[130:131]
